# speedup vs baseline: 1.0864x; 1.0114x over previous
_Z4k_lnPKfS0_S0_PDF16_PfS2_7CvtArgs:
	s_cmpk_lt_u32 s2, 0x100
	s_mov_b64 s[4:5], -1
	s_cbranch_scc0 .LBB0_8
	s_load_dwordx8 s[4:11], s[0:1], 0x0
	s_load_dwordx4 s[12:15], s[0:1], 0x20
	s_lshr_b32 s16, s2, 7
	s_lshl_b32 s3, s2, 5
	s_mov_b32 s17, 0
	s_and_b32 s3, s3, 0xfe0
	s_lshl_b64 s[18:19], s[16:17], 23
	v_and_b32_e32 v8, 0x1e0, v0
	v_and_b32_e32 v1, 31, v0
	v_lshlrev_b32_e32 v4, 2, v1
	v_mov_b32_e32 v5, 0
	v_lshl_add_u32 v9, v8, 14, v4
	v_lshlrev_b32_e32 v3, 2, v8
	v_mov_b32_e32 v6, 0
	v_mov_b32_e32 v7, 0
	s_waitcnt lgkmcnt(0)
	s_add_u32 s18, s4, s18
	s_addc_u32 s19, s5, s19
	s_lshl_b32 s4, s3, 2
	s_add_u32 s18, s18, s4
	s_addc_u32 s19, s19, 0
	global_load_dwordx4 v[66:69], v3, s[6:7]
	global_load_dwordx4 v[82:85], v3, s[8:9]
	global_load_dwordx4 v[70:73], v3, s[6:7] offset:16
	global_load_dwordx4 v[86:89], v3, s[8:9] offset:16
	global_load_dwordx4 v[74:77], v3, s[6:7] offset:32
	global_load_dwordx4 v[90:93], v3, s[8:9] offset:32
	global_load_dwordx4 v[78:81], v3, s[6:7] offset:48
	global_load_dwordx4 v[94:97], v3, s[8:9] offset:48
	global_load_dword v34, v9, s[18:19]
	s_add_u32 s18, s18, 0x4000
	s_addc_u32 s19, s19, 0
	global_load_dword v35, v9, s[18:19]
	s_add_u32 s18, s18, 0x4000
	s_addc_u32 s19, s19, 0
	global_load_dword v36, v9, s[18:19]
	s_add_u32 s18, s18, 0x4000
	s_addc_u32 s19, s19, 0
	global_load_dword v37, v9, s[18:19]
	s_add_u32 s18, s18, 0x4000
	s_addc_u32 s19, s19, 0
	global_load_dword v38, v9, s[18:19]
	s_add_u32 s18, s18, 0x4000
	s_addc_u32 s19, s19, 0
	global_load_dword v39, v9, s[18:19]
	s_add_u32 s18, s18, 0x4000
	s_addc_u32 s19, s19, 0
	global_load_dword v40, v9, s[18:19]
	s_add_u32 s18, s18, 0x4000
	s_addc_u32 s19, s19, 0
	global_load_dword v41, v9, s[18:19]
	s_add_u32 s18, s18, 0x4000
	s_addc_u32 s19, s19, 0
	global_load_dword v42, v9, s[18:19]
	s_add_u32 s18, s18, 0x4000
	s_addc_u32 s19, s19, 0
	global_load_dword v43, v9, s[18:19]
	s_add_u32 s18, s18, 0x4000
	s_addc_u32 s19, s19, 0
	global_load_dword v44, v9, s[18:19]
	s_add_u32 s18, s18, 0x4000
	s_addc_u32 s19, s19, 0
	global_load_dword v45, v9, s[18:19]
	s_add_u32 s18, s18, 0x4000
	s_addc_u32 s19, s19, 0
	global_load_dword v46, v9, s[18:19]
	s_add_u32 s18, s18, 0x4000
	s_addc_u32 s19, s19, 0
	global_load_dword v47, v9, s[18:19]
	s_add_u32 s18, s18, 0x4000
	s_addc_u32 s19, s19, 0
	global_load_dword v48, v9, s[18:19]
	s_add_u32 s18, s18, 0x4000
	s_addc_u32 s19, s19, 0
	global_load_dword v49, v9, s[18:19]
	s_add_u32 s18, s18, 0x4000
	s_addc_u32 s19, s19, 0
	global_load_dword v50, v9, s[18:19]
	s_add_u32 s18, s18, 0x4000
	s_addc_u32 s19, s19, 0
	global_load_dword v51, v9, s[18:19]
	s_add_u32 s18, s18, 0x4000
	s_addc_u32 s19, s19, 0
	global_load_dword v52, v9, s[18:19]
	s_add_u32 s18, s18, 0x4000
	s_addc_u32 s19, s19, 0
	global_load_dword v53, v9, s[18:19]
	s_add_u32 s18, s18, 0x4000
	s_addc_u32 s19, s19, 0
	global_load_dword v54, v9, s[18:19]
	s_add_u32 s18, s18, 0x4000
	s_addc_u32 s19, s19, 0
	global_load_dword v55, v9, s[18:19]
	s_add_u32 s18, s18, 0x4000
	s_addc_u32 s19, s19, 0
	global_load_dword v56, v9, s[18:19]
	s_add_u32 s18, s18, 0x4000
	s_addc_u32 s19, s19, 0
	global_load_dword v57, v9, s[18:19]
	s_add_u32 s18, s18, 0x4000
	s_addc_u32 s19, s19, 0
	global_load_dword v58, v9, s[18:19]
	s_add_u32 s18, s18, 0x4000
	s_addc_u32 s19, s19, 0
	global_load_dword v59, v9, s[18:19]
	s_add_u32 s18, s18, 0x4000
	s_addc_u32 s19, s19, 0
	global_load_dword v60, v9, s[18:19]
	s_add_u32 s18, s18, 0x4000
	s_addc_u32 s19, s19, 0
	global_load_dword v61, v9, s[18:19]
	s_add_u32 s18, s18, 0x4000
	s_addc_u32 s19, s19, 0
	global_load_dword v62, v9, s[18:19]
	s_add_u32 s18, s18, 0x4000
	s_addc_u32 s19, s19, 0
	global_load_dword v63, v9, s[18:19]
	s_add_u32 s18, s18, 0x4000
	s_addc_u32 s19, s19, 0
	global_load_dword v64, v9, s[18:19]
	s_add_u32 s18, s18, 0x4000
	s_addc_u32 s19, s19, 0
	global_load_dword v65, v9, s[18:19]
	s_waitcnt vmcnt(31)
	v_add_f32_e32 v6, v6, v34
	v_fmac_f32_e32 v7, v34, v34
	s_waitcnt vmcnt(30)
	v_add_f32_e32 v6, v6, v35
	v_fmac_f32_e32 v7, v35, v35
	s_waitcnt vmcnt(29)
	v_add_f32_e32 v6, v6, v36
	v_fmac_f32_e32 v7, v36, v36
	s_waitcnt vmcnt(28)
	v_add_f32_e32 v6, v6, v37
	v_fmac_f32_e32 v7, v37, v37
	s_waitcnt vmcnt(27)
	v_add_f32_e32 v6, v6, v38
	v_fmac_f32_e32 v7, v38, v38
	s_waitcnt vmcnt(26)
	v_add_f32_e32 v6, v6, v39
	v_fmac_f32_e32 v7, v39, v39
	s_waitcnt vmcnt(25)
	v_add_f32_e32 v6, v6, v40
	v_fmac_f32_e32 v7, v40, v40
	s_waitcnt vmcnt(24)
	v_add_f32_e32 v6, v6, v41
	v_fmac_f32_e32 v7, v41, v41
	s_waitcnt vmcnt(23)
	v_add_f32_e32 v6, v6, v42
	v_fmac_f32_e32 v7, v42, v42
	s_waitcnt vmcnt(22)
	v_add_f32_e32 v6, v6, v43
	v_fmac_f32_e32 v7, v43, v43
	s_waitcnt vmcnt(21)
	v_add_f32_e32 v6, v6, v44
	v_fmac_f32_e32 v7, v44, v44
	s_waitcnt vmcnt(20)
	v_add_f32_e32 v6, v6, v45
	v_fmac_f32_e32 v7, v45, v45
	s_waitcnt vmcnt(19)
	v_add_f32_e32 v6, v6, v46
	v_fmac_f32_e32 v7, v46, v46
	s_waitcnt vmcnt(18)
	v_add_f32_e32 v6, v6, v47
	v_fmac_f32_e32 v7, v47, v47
	s_waitcnt vmcnt(17)
	v_add_f32_e32 v6, v6, v48
	v_fmac_f32_e32 v7, v48, v48
	s_waitcnt vmcnt(16)
	v_add_f32_e32 v6, v6, v49
	v_fmac_f32_e32 v7, v49, v49
	s_waitcnt vmcnt(15)
	v_add_f32_e32 v6, v6, v50
	v_fmac_f32_e32 v7, v50, v50
	s_waitcnt vmcnt(14)
	v_add_f32_e32 v6, v6, v51
	v_fmac_f32_e32 v7, v51, v51
	s_waitcnt vmcnt(13)
	v_add_f32_e32 v6, v6, v52
	v_fmac_f32_e32 v7, v52, v52
	s_waitcnt vmcnt(12)
	v_add_f32_e32 v6, v6, v53
	v_fmac_f32_e32 v7, v53, v53
	s_waitcnt vmcnt(11)
	v_add_f32_e32 v6, v6, v54
	v_fmac_f32_e32 v7, v54, v54
	s_waitcnt vmcnt(10)
	v_add_f32_e32 v6, v6, v55
	v_fmac_f32_e32 v7, v55, v55
	s_waitcnt vmcnt(9)
	v_add_f32_e32 v6, v6, v56
	v_fmac_f32_e32 v7, v56, v56
	s_waitcnt vmcnt(8)
	v_add_f32_e32 v6, v6, v57
	v_fmac_f32_e32 v7, v57, v57
	s_waitcnt vmcnt(7)
	v_add_f32_e32 v6, v6, v58
	v_fmac_f32_e32 v7, v58, v58
	s_waitcnt vmcnt(6)
	v_add_f32_e32 v6, v6, v59
	v_fmac_f32_e32 v7, v59, v59
	s_waitcnt vmcnt(5)
	v_add_f32_e32 v6, v6, v60
	v_fmac_f32_e32 v7, v60, v60
	s_waitcnt vmcnt(4)
	v_add_f32_e32 v6, v6, v61
	v_fmac_f32_e32 v7, v61, v61
	s_waitcnt vmcnt(3)
	v_add_f32_e32 v6, v6, v62
	v_fmac_f32_e32 v7, v62, v62
	s_waitcnt vmcnt(2)
	v_add_f32_e32 v6, v6, v63
	v_fmac_f32_e32 v7, v63, v63
	s_waitcnt vmcnt(1)
	v_add_f32_e32 v6, v6, v64
	v_fmac_f32_e32 v7, v64, v64
	s_waitcnt vmcnt(0)
	v_add_f32_e32 v6, v6, v65
	v_fmac_f32_e32 v7, v65, v65
	v_lshlrev_b32_e32 v5, 2, v0
	s_movk_i32 s4, 0x780
	v_and_or_b32 v9, v5, s4, v4
	v_add_u32_e32 v9, 0x80, v9
	v_cmp_gt_u32_e32 vcc, 32, v0
	ds_write2st64_b32 v9, v7, v6 offset0:128 offset1:136
	s_waitcnt lgkmcnt(0)
	s_barrier
	s_and_saveexec_b64 s[18:19], vcc
	s_cbranch_execz .LBB0_5
	v_add_u32_e32 v9, 0x8800, v5
	ds_read2_b32 v[6:7], v9 offset0:32 offset1:64
	v_add_u32_e32 v18, 0x8000, v5
	ds_read2_b32 v[10:11], v18 offset0:32 offset1:64
	ds_read2_b32 v[12:13], v9 offset0:96 offset1:128
	ds_read2_b32 v[14:15], v18 offset0:96 offset1:128
	ds_read2_b32 v[16:17], v9 offset0:160 offset1:192
	ds_read2_b32 v[18:19], v18 offset0:160 offset1:192
	s_waitcnt lgkmcnt(4)
	v_mov_b32_e32 v20, v10
	v_add_u32_e32 v9, 0x8a00, v5
	v_mov_b32_e32 v21, v6
	v_pk_add_f32 v[20:21], v[20:21], 0 op_sel_hi:[1,0]
	v_mov_b32_e32 v6, v11
	v_pk_add_f32 v[6:7], v[20:21], v[6:7]
	s_waitcnt lgkmcnt(2)
	v_mov_b32_e32 v10, v14
	v_mov_b32_e32 v11, v12
	v_pk_add_f32 v[6:7], v[6:7], v[10:11]
	v_mov_b32_e32 v12, v15
	v_pk_add_f32 v[6:7], v[6:7], v[12:13]
	s_waitcnt lgkmcnt(0)
	v_mov_b32_e32 v10, v18
	v_mov_b32_e32 v11, v16
	v_pk_add_f32 v[6:7], v[6:7], v[10:11]
	ds_read2_b32 v[10:11], v9 offset0:96 offset1:128
	v_add_u32_e32 v9, 0x8200, v5
	ds_read2_b32 v[12:13], v9 offset0:96 offset1:128
	v_add_u32_e32 v9, 0x8c00, v5
	ds_read2_b32 v[14:15], v9 offset0:32 offset1:64
	v_add_u32_e32 v16, 0x8400, v5
	ds_read2_b32 v[20:21], v16 offset0:32 offset1:64
	ds_read2_b32 v[22:23], v9 offset0:96 offset1:128
	ds_read2_b32 v[24:25], v16 offset0:96 offset1:128
	ds_read2_b32 v[26:27], v9 offset0:160 offset1:192
	ds_read2_b32 v[28:29], v16 offset0:160 offset1:192
	v_mov_b32_e32 v16, v19
	v_pk_add_f32 v[6:7], v[6:7], v[16:17]
	s_waitcnt lgkmcnt(6)
	v_mov_b32_e32 v16, v12
	v_mov_b32_e32 v17, v10
	v_add_u32_e32 v9, 0x8e00, v5
	v_pk_add_f32 v[6:7], v[6:7], v[16:17]
	v_mov_b32_e32 v10, v13
	ds_read2_b32 v[30:31], v9 offset0:96 offset1:128
	v_add_u32_e32 v9, 0x8600, v5
	v_pk_add_f32 v[6:7], v[6:7], v[10:11]
	s_waitcnt lgkmcnt(5)
	v_mov_b32_e32 v10, v20
	v_mov_b32_e32 v11, v14
	ds_read2_b32 v[32:33], v9 offset0:96 offset1:128
	v_pk_add_f32 v[6:7], v[6:7], v[10:11]
	v_mov_b32_e32 v14, v21
	v_pk_add_f32 v[6:7], v[6:7], v[14:15]
	s_waitcnt lgkmcnt(4)
	v_mov_b32_e32 v10, v24
	v_mov_b32_e32 v11, v22
	v_pk_add_f32 v[6:7], v[6:7], v[10:11]
	v_mov_b32_e32 v22, v25
	v_pk_add_f32 v[6:7], v[6:7], v[22:23]
	s_waitcnt lgkmcnt(2)
	v_mov_b32_e32 v10, v28
	v_mov_b32_e32 v11, v26
	v_pk_add_f32 v[6:7], v[6:7], v[10:11]
	v_mov_b32_e32 v26, v29
	v_pk_add_f32 v[6:7], v[6:7], v[26:27]
	s_waitcnt lgkmcnt(0)
	v_mov_b32_e32 v10, v32
	v_mov_b32_e32 v11, v30
	v_pk_add_f32 v[6:7], v[6:7], v[10:11]
	v_mov_b32_e32 v30, v33
	v_pk_add_f32 v[6:7], v[6:7], v[30:31]
	s_mov_b32 s4, 0x3b000000
	v_pk_mul_f32 v[6:7], v[6:7], s[4:5] op_sel_hi:[1,0]
	s_mov_b32 s4, 0xf800000
	v_fma_f32 v6, -v7, v7, v6
	v_cmp_ngt_f32_e32 vcc, 0, v6
	v_add_u32_e32 v5, 0x9000, v5
	s_nop 0
	v_cndmask_b32_e32 v6, 0, v6, vcc
	v_add_f32_e32 v6, 0x3727c5ac, v6
	v_mul_f32_e32 v9, 0x4f800000, v6
	v_cmp_gt_f32_e32 vcc, s4, v6
	s_nop 1
	v_cndmask_b32_e32 v6, v6, v9, vcc
	v_sqrt_f32_e32 v9, v6
	s_nop 0
	v_add_u32_e32 v10, -1, v9
	v_fma_f32 v11, -v10, v9, v6
	v_cmp_ge_f32_e64 s[4:5], 0, v11
	v_add_u32_e32 v11, 1, v9
	s_nop 0
	v_cndmask_b32_e64 v10, v9, v10, s[4:5]
	v_fma_f32 v9, -v11, v9, v6
	v_cmp_lt_f32_e64 s[4:5], 0, v9
	s_nop 1
	v_cndmask_b32_e64 v9, v10, v11, s[4:5]
	v_mul_f32_e32 v10, 0x37800000, v9
	v_cndmask_b32_e32 v9, v9, v10, vcc
	v_mov_b32_e32 v10, 0x260
	v_cmp_class_f32_e32 vcc, v6, v10
	s_nop 1
	v_cndmask_b32_e32 v6, v9, v6, vcc
	v_div_scale_f32 v9, s[4:5], v6, v6, 1.0
	v_rcp_f32_e32 v10, v9
	s_lshl_b32 s4, s16, 12
	s_or_b32 s4, s4, s3
	v_fma_f32 v11, -v9, v10, 1.0
	v_fmac_f32_e32 v10, v11, v10
	v_div_scale_f32 v11, vcc, 1.0, v6, 1.0
	v_mul_f32_e32 v12, v11, v10
	v_fma_f32 v13, -v9, v12, v11
	v_fmac_f32_e32 v12, v13, v10
	v_fma_f32 v9, -v9, v12, v11
	v_div_fmas_f32 v9, v9, v10, v12
	v_or_b32_e32 v10, s4, v0
	v_mov_b32_e32 v11, 0
	v_lshlrev_b64 v[10:11], 2, v[10:11]
	v_div_fixup_f32 v9, v9, v6, 1.0
	v_lshl_add_u64 v[12:13], s[12:13], 0, v[10:11]
	ds_write2_b32 v5, v7, v9 offset0:32 offset1:64
	global_store_dword v[12:13], v7, off
	v_lshl_add_u64 v[6:7], s[14:15], 0, v[10:11]
	global_store_dword v[6:7], v9, off
.LBB0_5:
	s_or_b64 exec, exec, s[18:19]
	global_load_dwordx4 v[98:101], v3, s[6:7] offset:64
	global_load_dwordx4 v[22:25], v3, s[8:9] offset:64
	global_load_dwordx4 v[102:105], v3, s[6:7] offset:80
	global_load_dwordx4 v[26:29], v3, s[8:9] offset:80
	global_load_dwordx4 v[106:109], v3, s[6:7] offset:96
	global_load_dwordx4 v[30:33], v3, s[8:9] offset:96
	global_load_dwordx4 v[110:113], v3, s[6:7] offset:112
	global_load_dwordx4 v[114:117], v3, s[8:9] offset:112
	s_waitcnt lgkmcnt(0)
	s_barrier
	v_add_u32_e32 v4, 0x9000, v4
	ds_read2_b32 v[6:7], v4 offset0:32 offset1:64
	v_lshlrev_b32_e32 v8, 1, v8
	s_movk_i32 s12, 0x404
	v_mad_u32_u24 v1, v1, s12, v8
	s_lshl_b64 s[4:5], s[16:17], 22
	s_add_u32 s4, s10, s4
	s_addc_u32 s5, s11, s5
	s_lshl_b32 s3, s3, 10
	s_add_u32 s4, s4, s3
	s_addc_u32 s5, s5, 0
	s_waitcnt lgkmcnt(0)
	v_mov_b32_e32 v4, v7
	s_nop 0
	v_pk_add_f32 v[10:11], v[34:35], v[6:7] op_sel_hi:[1,0] neg_lo:[0,1] neg_hi:[0,1]
	v_pk_add_f32 v[12:13], v[36:37], v[6:7] op_sel_hi:[1,0] neg_lo:[0,1] neg_hi:[0,1]
	v_pk_add_f32 v[14:15], v[38:39], v[6:7] op_sel_hi:[1,0] neg_lo:[0,1] neg_hi:[0,1]
	v_pk_add_f32 v[16:17], v[40:41], v[6:7] op_sel_hi:[1,0] neg_lo:[0,1] neg_hi:[0,1]
	v_pk_mul_f32 v[10:11], v[4:5], v[10:11] op_sel_hi:[0,1]
	v_pk_mul_f32 v[12:13], v[4:5], v[12:13] op_sel_hi:[0,1]
	v_pk_mul_f32 v[14:15], v[4:5], v[14:15] op_sel_hi:[0,1]
	v_pk_mul_f32 v[16:17], v[4:5], v[16:17] op_sel_hi:[0,1]
	v_pk_fma_f32 v[10:11], v[66:67], v[10:11], v[82:83]
	v_pk_fma_f32 v[12:13], v[68:69], v[12:13], v[84:85]
	v_pk_fma_f32 v[14:15], v[70:71], v[14:15], v[86:87]
	v_pk_fma_f32 v[16:17], v[72:73], v[16:17], v[88:89]
	v_cvt_pk_f16_f32 v18, v10, v11
	v_cvt_pk_f16_f32 v19, v12, v13
	v_cvt_pk_f16_f32 v20, v14, v15
	v_cvt_pk_f16_f32 v21, v16, v17
	ds_write2_b32 v1, v18, v19 offset0:0 offset1:1
	ds_write2_b32 v1, v20, v21 offset0:2 offset1:3
	v_pk_add_f32 v[10:11], v[42:43], v[6:7] op_sel_hi:[1,0] neg_lo:[0,1] neg_hi:[0,1]
	v_pk_add_f32 v[12:13], v[44:45], v[6:7] op_sel_hi:[1,0] neg_lo:[0,1] neg_hi:[0,1]
	v_pk_add_f32 v[14:15], v[46:47], v[6:7] op_sel_hi:[1,0] neg_lo:[0,1] neg_hi:[0,1]
	v_pk_add_f32 v[16:17], v[48:49], v[6:7] op_sel_hi:[1,0] neg_lo:[0,1] neg_hi:[0,1]
	v_pk_mul_f32 v[10:11], v[4:5], v[10:11] op_sel_hi:[0,1]
	v_pk_mul_f32 v[12:13], v[4:5], v[12:13] op_sel_hi:[0,1]
	v_pk_mul_f32 v[14:15], v[4:5], v[14:15] op_sel_hi:[0,1]
	v_pk_mul_f32 v[16:17], v[4:5], v[16:17] op_sel_hi:[0,1]
	v_pk_fma_f32 v[10:11], v[74:75], v[10:11], v[90:91]
	v_pk_fma_f32 v[12:13], v[76:77], v[12:13], v[92:93]
	v_pk_fma_f32 v[14:15], v[78:79], v[14:15], v[94:95]
	v_pk_fma_f32 v[16:17], v[80:81], v[16:17], v[96:97]
	v_cvt_pk_f16_f32 v18, v10, v11
	v_cvt_pk_f16_f32 v19, v12, v13
	v_cvt_pk_f16_f32 v20, v14, v15
	v_cvt_pk_f16_f32 v21, v16, v17
	ds_write2_b32 v1, v18, v19 offset0:4 offset1:5
	ds_write2_b32 v1, v20, v21 offset0:6 offset1:7
	s_waitcnt vmcnt(0)
	v_pk_add_f32 v[10:11], v[50:51], v[6:7] op_sel_hi:[1,0] neg_lo:[0,1] neg_hi:[0,1]
	v_pk_add_f32 v[12:13], v[52:53], v[6:7] op_sel_hi:[1,0] neg_lo:[0,1] neg_hi:[0,1]
	v_pk_add_f32 v[14:15], v[54:55], v[6:7] op_sel_hi:[1,0] neg_lo:[0,1] neg_hi:[0,1]
	v_pk_add_f32 v[16:17], v[56:57], v[6:7] op_sel_hi:[1,0] neg_lo:[0,1] neg_hi:[0,1]
	v_pk_mul_f32 v[10:11], v[4:5], v[10:11] op_sel_hi:[0,1]
	v_pk_mul_f32 v[12:13], v[4:5], v[12:13] op_sel_hi:[0,1]
	v_pk_mul_f32 v[14:15], v[4:5], v[14:15] op_sel_hi:[0,1]
	v_pk_mul_f32 v[16:17], v[4:5], v[16:17] op_sel_hi:[0,1]
	v_pk_fma_f32 v[10:11], v[98:99], v[10:11], v[22:23]
	v_pk_fma_f32 v[12:13], v[100:101], v[12:13], v[24:25]
	v_pk_fma_f32 v[14:15], v[102:103], v[14:15], v[26:27]
	v_pk_fma_f32 v[16:17], v[104:105], v[16:17], v[28:29]
	v_cvt_pk_f16_f32 v18, v10, v11
	v_cvt_pk_f16_f32 v19, v12, v13
	v_cvt_pk_f16_f32 v20, v14, v15
	v_cvt_pk_f16_f32 v21, v16, v17
	ds_write2_b32 v1, v18, v19 offset0:8 offset1:9
	ds_write2_b32 v1, v20, v21 offset0:10 offset1:11
	v_pk_add_f32 v[10:11], v[58:59], v[6:7] op_sel_hi:[1,0] neg_lo:[0,1] neg_hi:[0,1]
	v_pk_add_f32 v[12:13], v[60:61], v[6:7] op_sel_hi:[1,0] neg_lo:[0,1] neg_hi:[0,1]
	v_pk_add_f32 v[14:15], v[62:63], v[6:7] op_sel_hi:[1,0] neg_lo:[0,1] neg_hi:[0,1]
	v_pk_add_f32 v[16:17], v[64:65], v[6:7] op_sel_hi:[1,0] neg_lo:[0,1] neg_hi:[0,1]
	v_pk_mul_f32 v[10:11], v[4:5], v[10:11] op_sel_hi:[0,1]
	v_pk_mul_f32 v[12:13], v[4:5], v[12:13] op_sel_hi:[0,1]
	v_pk_mul_f32 v[14:15], v[4:5], v[14:15] op_sel_hi:[0,1]
	v_pk_mul_f32 v[16:17], v[4:5], v[16:17] op_sel_hi:[0,1]
	v_pk_fma_f32 v[10:11], v[106:107], v[10:11], v[30:31]
	v_pk_fma_f32 v[12:13], v[108:109], v[12:13], v[32:33]
	v_pk_fma_f32 v[14:15], v[110:111], v[14:15], v[114:115]
	v_pk_fma_f32 v[16:17], v[112:113], v[16:17], v[116:117]
	v_cvt_pk_f16_f32 v18, v10, v11
	v_cvt_pk_f16_f32 v19, v12, v13
	v_cvt_pk_f16_f32 v20, v14, v15
	v_cvt_pk_f16_f32 v21, v16, v17
	ds_write2_b32 v1, v18, v19 offset0:12 offset1:13
	ds_write2_b32 v1, v20, v21 offset0:14 offset1:15
	s_waitcnt lgkmcnt(0)
	s_barrier
	v_lshrrev_b32_e32 v1, 6, v0
	v_and_b32_e32 v2, 63, v0
	v_mul_u32_u24_e32 v1, 0x404, v1
	v_lshl_add_u32 v1, v2, 4, v1
	v_lshlrev_b32_e32 v3, 4, v0
	ds_read2_b32 v[4:5], v1 offset1:1
	ds_read2_b32 v[6:7], v1 offset0:2 offset1:3
	v_add_u32_e32 v1, 0x2020, v1
	ds_read2_b32 v[8:9], v1 offset1:1
	ds_read2_b32 v[10:11], v1 offset0:2 offset1:3
	v_add_u32_e32 v1, 0x2020, v1
	ds_read2_b32 v[12:13], v1 offset1:1
	ds_read2_b32 v[14:15], v1 offset0:2 offset1:3
	v_add_u32_e32 v1, 0x2020, v1
	ds_read2_b32 v[16:17], v1 offset1:1
	ds_read2_b32 v[18:19], v1 offset0:2 offset1:3
	s_waitcnt lgkmcnt(6)
	global_store_dwordx4 v3, v[4:7], s[4:5] sc1
	v_add_u32_e32 v3, 0x2000, v3
	s_waitcnt lgkmcnt(4)
	global_store_dwordx4 v3, v[8:11], s[4:5] sc1
	v_add_u32_e32 v3, 0x2000, v3
	s_waitcnt lgkmcnt(2)
	global_store_dwordx4 v3, v[12:15], s[4:5] sc1
	v_add_u32_e32 v3, 0x2000, v3
	s_waitcnt lgkmcnt(0)
	global_store_dwordx4 v3, v[16:19], s[4:5] sc1
	s_mov_b64 s[4:5], 0

	.amdhsa_kernel _Z4k_lnPKfS0_S0_PDF16_PfS2_7CvtArgs
		.amdhsa_group_segment_fixed_size 37248
		.amdhsa_private_segment_fixed_size 0
		.amdhsa_kernarg_size 152
		.amdhsa_user_sgpr_count 2
		.amdhsa_user_sgpr_dispatch_ptr 0
		.amdhsa_user_sgpr_queue_ptr 0
		.amdhsa_user_sgpr_kernarg_segment_ptr 1
		.amdhsa_user_sgpr_dispatch_id 0
		.amdhsa_user_sgpr_kernarg_preload_length 0
		.amdhsa_user_sgpr_kernarg_preload_offset 0
		.amdhsa_user_sgpr_private_segment_size 0
		.amdhsa_uses_dynamic_stack 0
		.amdhsa_enable_private_segment 0
		.amdhsa_system_sgpr_workgroup_id_x 1
		.amdhsa_system_sgpr_workgroup_id_y 0
		.amdhsa_system_sgpr_workgroup_id_z 0
		.amdhsa_system_sgpr_workgroup_info 0
		.amdhsa_system_vgpr_workitem_id 0
		.amdhsa_next_free_vgpr 118
		.amdhsa_next_free_sgpr 34
		.amdhsa_accum_offset 120
		.amdhsa_reserve_vcc 1
		.amdhsa_float_round_mode_32 0
		.amdhsa_float_round_mode_16_64 0
		.amdhsa_float_denorm_mode_32 3
		.amdhsa_float_denorm_mode_16_64 3
		.amdhsa_dx10_clamp 1
		.amdhsa_ieee_mode 1
		.amdhsa_fp16_overflow 0
		.amdhsa_tg_split 0
		.amdhsa_exception_fp_ieee_invalid_op 0
		.amdhsa_exception_fp_denorm_src 0
		.amdhsa_exception_fp_ieee_div_zero 0
		.amdhsa_exception_fp_ieee_overflow 0
		.amdhsa_exception_fp_ieee_underflow 0
		.amdhsa_exception_fp_ieee_inexact 0
		.amdhsa_exception_int_div_zero 0
	.end_amdhsa_kernel

amdhsa.kernels:
  - .agpr_count:     0
    .args:
      - .actual_access:  read_only
        .address_space:  global
        .offset:         0
        .size:           8
        .value_kind:     global_buffer
      - .actual_access:  read_only
        .address_space:  global
        .offset:         8
        .size:           8
        .value_kind:     global_buffer
      - .actual_access:  read_only
        .address_space:  global
        .offset:         16
        .size:           8
        .value_kind:     global_buffer
      - .actual_access:  write_only
        .address_space:  global
        .offset:         24
        .size:           8
        .value_kind:     global_buffer
      - .actual_access:  write_only
        .address_space:  global
        .offset:         32
        .size:           8
        .value_kind:     global_buffer
      - .actual_access:  write_only
        .address_space:  global
        .offset:         40
        .size:           8
        .value_kind:     global_buffer
      - .offset:         48
        .size:           104
        .value_kind:     by_value
    .group_segment_fixed_size: 37248
    .kernarg_segment_align: 8
    .kernarg_segment_size: 152
    .language:       OpenCL C
    .language_version:
      - 2
      - 0
    .max_flat_workgroup_size: 512
    .name:           _Z4k_lnPKfS0_S0_PDF16_PfS2_7CvtArgs
    .private_segment_fixed_size: 0
    .sgpr_count:     40
    .sgpr_spill_count: 0
    .symbol:         _Z4k_lnPKfS0_S0_PDF16_PfS2_7CvtArgs.kd
    .uniform_work_group_size: 1
    .uses_dynamic_stack: false
    .vgpr_count:     118
    .vgpr_spill_count: 0
    .wavefront_size: 64
  - .agpr_count:     36
    .args:
      - .actual_access:  read_only
        .address_space:  global
        .offset:         0
        .size:           8
        .value_kind:     global_buffer
      - .actual_access:  read_only
        .address_space:  global
        .offset:         8
        .size:           8
        .value_kind:     global_buffer
      - .actual_access:  read_only
        .address_space:  global
        .offset:         16
        .size:           8
        .value_kind:     global_buffer
      - .actual_access:  read_only
        .address_space:  global
        .offset:         24
        .size:           8
        .value_kind:     global_buffer
      - .actual_access:  read_only
        .address_space:  global
        .offset:         32
        .size:           8
        .value_kind:     global_buffer
      - .actual_access:  read_only
        .address_space:  global
        .offset:         40
        .size:           8
        .value_kind:     global_buffer
      - .actual_access:  read_only
        .address_space:  global
        .offset:         48
        .size:           8
        .value_kind:     global_buffer
      - .actual_access:  read_only
        .address_space:  global
        .offset:         56
        .size:           8
        .value_kind:     global_buffer
      - .actual_access:  write_only
        .address_space:  global
        .offset:         64
        .size:           8
        .value_kind:     global_buffer
      - .actual_access:  write_only
        .address_space:  global
        .offset:         72
        .size:           8
        .value_kind:     global_buffer
      - .actual_access:  write_only
        .address_space:  global
        .offset:         80
        .size:           8
        .value_kind:     global_buffer
      - .actual_access:  write_only
        .address_space:  global
        .offset:         88
        .size:           8
        .value_kind:     global_buffer
      - .actual_access:  write_only
        .address_space:  global
        .offset:         96
        .size:           8
        .value_kind:     global_buffer
    .group_segment_fixed_size: 77312
    .kernarg_segment_align: 8
    .kernarg_segment_size: 104
    .language:       OpenCL C
    .language_version:
      - 2
      - 0
    .max_flat_workgroup_size: 256
    .name:           _Z7k_frontPKDF16_S0_PKfS2_S0_S2_S2_S2_PjPfS4_S4_S4_
    .private_segment_fixed_size: 0
    .sgpr_count:     25
    .sgpr_spill_count: 0
    .symbol:         _Z7k_frontPKDF16_S0_PKfS2_S0_S2_S2_S2_PjPfS4_S4_S4_.kd
    .uniform_work_group_size: 1
    .uses_dynamic_stack: false
    .vgpr_count:     204
    .vgpr_spill_count: 0
    .wavefront_size: 64
  - .agpr_count:     0
    .args:
      - .actual_access:  read_only
        .address_space:  global
        .offset:         0
        .size:           8
        .value_kind:     global_buffer
      - .address_space:  global
        .offset:         8
        .size:           8
        .value_kind:     global_buffer
      - .actual_access:  read_only
        .address_space:  global
        .offset:         16
        .size:           8
        .value_kind:     global_buffer
    .group_segment_fixed_size: 0
    .kernarg_segment_align: 8
    .kernarg_segment_size: 24
    .language:       OpenCL C
    .language_version:
      - 2
      - 0
    .max_flat_workgroup_size: 64
    .name:           _Z7k_scan2PKfPfS0_
    .private_segment_fixed_size: 0
    .sgpr_count:     48
    .sgpr_spill_count: 0
    .symbol:         _Z7k_scan2PKfPfS0_.kd
    .uniform_work_group_size: 1
    .uses_dynamic_stack: false
    .vgpr_count:     150
    .vgpr_spill_count: 0
    .wavefront_size: 64
  - .agpr_count:     0
    .args:
      - .actual_access:  read_only
        .address_space:  global
        .offset:         0
        .size:           8
        .value_kind:     global_buffer
      - .actual_access:  read_only
        .address_space:  global
        .offset:         8
        .size:           8
        .value_kind:     global_buffer
      - .actual_access:  read_only
        .address_space:  global
        .offset:         16
        .size:           8
        .value_kind:     global_buffer
      - .actual_access:  read_only
        .address_space:  global
        .offset:         24
        .size:           8
        .value_kind:     global_buffer
      - .actual_access:  read_only
        .address_space:  global
        .offset:         32
        .size:           8
        .value_kind:     global_buffer
      - .actual_access:  read_only
        .address_space:  global
        .offset:         40
        .size:           8
        .value_kind:     global_buffer
      - .actual_access:  read_only
        .address_space:  global
        .offset:         48
        .size:           8
        .value_kind:     global_buffer
      - .actual_access:  read_only
        .address_space:  global
        .offset:         56
        .size:           8
        .value_kind:     global_buffer
      - .actual_access:  read_only
        .address_space:  global
        .offset:         64
        .size:           8
        .value_kind:     global_buffer
      - .offset:         72
        .size:           72
        .value_kind:     by_value
    .group_segment_fixed_size: 60416
    .kernarg_segment_align: 8
    .kernarg_segment_size: 144
    .language:       OpenCL C
    .language_version:
      - 2
      - 0
    .max_flat_workgroup_size: 256
    .name:           _Z7k_scan3PKjPKfS2_S2_S2_S2_PKDF16_S4_S4_7EpiArgs
    .private_segment_fixed_size: 0
    .sgpr_count:     34
    .sgpr_spill_count: 0
    .symbol:         _Z7k_scan3PKjPKfS2_S2_S2_S2_PKDF16_S4_S4_7EpiArgs.kd
    .uniform_work_group_size: 1
    .uses_dynamic_stack: false
    .vgpr_count:     236
    .vgpr_spill_count: 0
    .wavefront_size: 64
  - .agpr_count:     0
    .args:
      - .actual_access:  read_only
        .address_space:  global
        .offset:         0
        .size:           8
        .value_kind:     global_buffer
      - .actual_access:  read_only
        .address_space:  global
        .offset:         8
        .size:           8
        .value_kind:     global_buffer
      - .actual_access:  read_only
        .address_space:  global
        .offset:         16
        .size:           8
        .value_kind:     global_buffer
      - .actual_access:  write_only
        .address_space:  global
        .offset:         24
        .size:           8
        .value_kind:     global_buffer
    .group_segment_fixed_size: 20160
    .kernarg_segment_align: 8
    .kernarg_segment_size: 32
    .language:       OpenCL C
    .language_version:
      - 2
      - 0
    .max_flat_workgroup_size: 256
    .name:           _Z8k_dwconvPKDF16_PKfS2_PDF16_
    .private_segment_fixed_size: 0
    .sgpr_count:     86
    .sgpr_spill_count: 0
    .symbol:         _Z8k_dwconvPKDF16_PKfS2_PDF16_.kd
    .uniform_work_group_size: 1
    .uses_dynamic_stack: false
    .vgpr_count:     65
    .vgpr_spill_count: 0
    .wavefront_size: 64
  - .agpr_count:     0
    .args:
      - .actual_access:  read_only
        .address_space:  global
        .offset:         0
        .size:           8
        .value_kind:     global_buffer
      - .offset:         8
        .size:           72
        .value_kind:     by_value
    .group_segment_fixed_size: 38912
    .kernarg_segment_align: 8
    .kernarg_segment_size: 80
    .language:       OpenCL C
    .language_version:
      - 2
      - 0
    .max_flat_workgroup_size: 256
    .name:           _Z9k_gemm_tlILi2ELb1EEvPKDF16_6TlArgs
    .private_segment_fixed_size: 0
    .sgpr_count:     27
    .sgpr_spill_count: 0
    .symbol:         _Z9k_gemm_tlILi2ELb1EEvPKDF16_6TlArgs.kd
    .uniform_work_group_size: 1
    .uses_dynamic_stack: false
    .vgpr_count:     124
    .vgpr_spill_count: 0
    .wavefront_size: 64
  - .agpr_count:     0
    .args:
      - .actual_access:  read_only
        .address_space:  global
        .offset:         0
        .size:           8
        .value_kind:     global_buffer
      - .offset:         8
        .size:           72
        .value_kind:     by_value
    .group_segment_fixed_size: 34816
    .kernarg_segment_align: 8
    .kernarg_segment_size: 80
    .language:       OpenCL C
    .language_version:
      - 2
      - 0
    .max_flat_workgroup_size: 256
    .name:           _Z9k_gemm_tlILi3ELb0EEvPKDF16_6TlArgs
    .private_segment_fixed_size: 0
    .sgpr_count:     18
    .sgpr_spill_count: 0
    .symbol:         _Z9k_gemm_tlILi3ELb0EEvPKDF16_6TlArgs.kd
    .uniform_work_group_size: 1
    .uses_dynamic_stack: false
    .vgpr_count:     110
    .vgpr_spill_count: 0
    .wavefront_size: 64
